# v3_prio
# speedup vs baseline: 1.0470x; 1.0105x over previous
.LBB1_50:
	s_or_b64 exec, exec, s[0:1]
	v_and_b32_e32 v1, 31, v0
	v_lshrrev_b32_e32 v24, 8, v0
	v_mad_u32_u24 v19, v24, 42, v1
	v_min_u32_e32 v20, 0x53, v19
	v_lshrrev_b32_e32 v18, 5, v193
	s_movk_i32 s64, 0x110
	v_mul_u32_u24_e32 v25, 0x110, v20
	v_min_u32_e32 v20, 62, v19
	v_lshlrev_b32_e32 v206, 6, v189
	v_mov_b32_e32 v66, 0
	v_mul_u32_u24_e32 v26, 0x110, v20
	v_lshlrev_b32_e32 v204, 4, v18
	v_mad_u32_u24 v22, v19, s64, v206
	v_lshlrev_b32_e32 v27, 3, v18
	v_lshlrev_b32_e32 v18, 1, v183
	v_mov_b32_e32 v19, v66
	v_lshlrev_b32_e32 v20, 10, v185
	v_lshl_add_u64 v[18:19], s[30:31], 0, v[18:19]
	v_and_b32_e32 v20, 0x1000, v20
	v_mov_b32_e32 v21, v66
	v_lshl_add_u64 v[18:19], v[18:19], 0, v[20:21]
	v_mov_b32_e32 v183, v66
	v_lshl_add_u64 v[18:19], v[18:19], 0, v[182:183]
	s_mov_b64 s[6:7], 0x48000
	v_lshl_add_u64 v[208:209], v[18:19], 0, s[6:7]
	v_lshrrev_b32_e32 v18, 2, v0
	v_and_b32_e32 v29, 8, v18
	v_mul_u32_u24_e32 v18, 0x3000, v189
	v_lshlrev_b32_e32 v210, 2, v193
	v_or_b32_e32 v18, v18, v210
	v_add_u32_e32 v221, 0x15a80, v18
	v_lshlrev_b32_e32 v18, 6, v193
	v_and_b32_e32 v20, 0xe00, v18
	s_add_u32 s34, s18, 0xc000
	s_movk_i32 s3, 0xff
	v_add_u32_e32 v19, 0x25a80, v210
	v_and_b32_e32 v224, 0x800, v18
	v_or_b32_e32 v225, 0x6600, v20
	v_or_b32_e32 v226, 0x7600, v20
	v_or_b32_e32 v227, 0x8600, v20
	v_or_b32_e32 v228, 0x9600, v20
	v_or_b32_e32 v229, 0x600, v20
	v_or_b32_e32 v230, 0x1600, v20
	v_or_b32_e32 v231, 0x2600, v20
	v_or_b32_e32 v232, 0x3600, v20
	v_or_b32_e32 v233, 0x4600, v20
	v_or_b32_e32 v234, 0x5600, v20
	v_lshlrev_b32_e32 v18, 8, v189
	v_lshlrev_b32_e32 v20, 2, v0
	s_addc_u32 s35, s19, 0
	v_cmp_lt_u32_e64 s[6:7], s3, v0
	v_and_b32_e32 v32, 0x7c, v20
	s_lshl_b32 s3, s2, 3
	v_add_u32_e32 v236, v19, v18
	s_lshl_b32 s2, s2, 5
	v_lshlrev_b32_e32 v18, 14, v185
	v_mov_b32_e32 v19, v66
	v_lshlrev_b32_e32 v20, 15, v189
	v_add_u32_e32 v28, 0x10140, v22
	v_add_u32_e32 v30, 0x11790, v22
	s_and_b32 s67, s3, 0x700
	s_and_b32 s2, s2, 0x1f00
	v_lshl_add_u64 v[18:19], s[30:31], 0, v[18:19]
	v_lshl_add_u64 v[20:21], s[30:31], 0, v[20:21]
	v_lshlrev_b32_e32 v22, 14, v24
	v_mov_b32_e32 v23, v66
	s_add_u32 s38, s34, s2
	v_lshl_add_u64 v[18:19], v[18:19], 0, v[182:183]
	s_mov_b64 s[2:3], 0x60000
	v_lshl_add_u64 v[20:21], v[20:21], 0, v[22:23]
	v_or_b32_e32 v220, v212, v1
	v_lshl_add_u64 v[212:213], v[18:19], 0, s[2:3]
	v_lshl_add_u64 v[20:21], v[20:21], 0, v[182:183]
	s_mov_b64 s[2:3], 0xc0000
	v_lshlrev_b32_e32 v33, 7, v185
	v_lshl_add_u64 v[214:215], v[20:21], 0, s[2:3]
	v_or_b32_e32 v23, 64, v1
	s_movk_i32 s69, 0x410
	v_mov_b32_e32 v20, 0x10140
	v_or_b32_e32 v237, v33, v32
	v_and_b32_e32 v18, 0x1c0, v0
	v_or_b32_e32 v22, v27, v33
	v_mad_u32_u24 v33, v23, s69, v20
	v_lshlrev_b32_e32 v20, 2, v32
	v_mov_b32_e32 v21, v66
	v_or_b32_e32 v31, 0x10140, v204
	v_lshlrev_b32_e32 v18, 2, v18
	v_mov_b32_e32 v19, v66
	s_movk_i32 s68, 0x54
	v_lshl_add_u64 v[216:217], s[26:27], 0, v[20:21]
	v_or_b32_e32 v20, 32, v1
	v_min_i32_e32 v21, 0x53, v23
	s_mov_b32 s37, 0
	v_lshl_or_b32 v207, v24, 7, v31
	v_cmp_eq_u32_e64 s[8:9], 1, v24
	v_lshlrev_b32_e32 v222, 2, v220
	v_lshl_add_u64 v[18:19], s[16:17], 0, v[18:19]
	v_cmp_gt_u32_e64 s[12:13], s68, v23
	v_lshl_or_b32 v24, v24, 9, v31
	v_mul_u32_u24_e32 v20, 0x110, v20
	v_mul_u32_u24_e32 v23, 0x110, v21
	v_mul_u32_u24_e32 v31, 0x410, v1
	v_mul_u32_u24_e32 v21, 0x410, v21
	v_mov_b32_e32 v205, v66
	s_mov_b32 s16, 0x18618618
	v_cmp_gt_u32_e64 s[0:1], 32, v193
	v_cmp_lt_u32_e64 s[14:15], 31, v193
	v_cmp_gt_u32_e64 s[4:5], 21, v1
	s_movk_i32 s65, 0x1000
	s_movk_i32 s66, 0x3000
	v_add_u32_e32 v223, 0x25680, v222
	v_lshl_or_b32 v235, v189, 7, v32
	v_cmp_eq_u32_e64 s[10:11], 0, v193
	s_addc_u32 s39, s35, 0
	v_mul_u32_u24_e32 v238, 0x110, v1
	v_add_u32_e32 v239, 0x10140, v22
	s_add_i32 s70, s33, 16
	s_add_i32 s71, s33, 32
	s_add_i32 s72, s33, 48
	s_add_i32 s73, s33, 64
	s_add_i32 s74, s33, 0x50
	v_lshl_add_u64 v[218:219], v[18:19], 0, v[204:205]
	v_add_u32_e32 v205, v25, v184
	v_add_u32_e32 v240, v26, v204
	v_add_u32_e32 v241, v207, v20
	v_add_u32_e32 v242, v207, v23
	s_movk_i32 s75, 0x2000
	s_movk_i32 s76, 0x100
	s_movk_i32 s77, 0xffc0
	s_mov_b32 s17, 0x3f086186
	s_mov_b32 s78, 0xf800000
	v_mov_b32_e32 v243, 0x260
	s_movk_i32 s79, 0x44
	v_add_u32_e32 v244, v33, v22
	v_add_u32_e32 v245, v24, v31
	v_add_u32_e32 v246, v24, v21
	v_add_u32_e32 v247, v28, v27
	v_add_u32_e32 v248, v30, v29
	v_mov_b32_e32 v249, 0x25680
	s_mov_b32 s36, s37
	s_cmp_eq_u64 s[6:7], 0
	s_cbranch_scc0 .Lprio_skip
	s_setprio 1
.Lprio_skip:
	s_waitcnt lgkmcnt(0)
	s_barrier
	s_branch .LBB1_53
